# stagger: waves 4-7 s_sleep 8 after DMA issue in 4 attention tile loops
# speedup vs baseline: 1.0017x; 1.0017x over previous
.LBB0_3607:
	s_or_b64 exec, exec, s[4:5]
	v_mov_b32_e32 v0, s59
	s_waitcnt lgkmcnt(0)
	s_barrier
	ds_read_b32 v0, v0
	v_readlane_b32 s2, v254, 55
	v_readlane_b32 s3, v254, 56
	s_xor_b64 s[40:41], s[2:3], -1
	s_waitcnt lgkmcnt(0)
	v_readfirstlane_b32 s69, v0
	s_cmpk_gt_i32 s69, 0x67f
	s_cselect_b64 s[86:87], -1, 0
	s_and_b64 vcc, exec, s[86:87]
	s_barrier
	s_cbranch_vccnz .LBB0_3602
	v_mov_b32_e32 v154, v147
	s_mov_b64 s[6:7], -1
	v_readfirstlane_b32 s33, v154
	s_ashr_i32 s79, s33, 6
	s_lshr_b32 s99, s79, 2
	v_and_b32_e32 v153, 63, v154
	s_cmpk_gt_i32 s69, 0x7f
	s_cbranch_scc0 .LBB0_3774
	s_add_i32 s48, s69, 0xfffffd80
	s_cmpk_gt_u32 s48, 0x1ff
	s_mov_b64 s[4:5], -1
	s_cbranch_scc0 .LBB0_3657
	s_cmpk_gt_u32 s69, 0x27f
	s_cbranch_scc0 .LBB0_3635
	s_cmpk_lt_u32 s69, 0x480
	s_cbranch_scc1 .LBB0_3634
	v_readlane_b32 s2, v254, 58
	v_readlane_b32 s3, v254, 59
	s_load_dwordx2 s[4:5], s[2:3], 0x28
	s_add_i32 s0, s69, 0xfffffb80
	s_lshr_b32 s6, s0, 4
	s_sub_i32 s2, 31, s6
	v_readlane_b32 s8, v255, 34
	v_readlane_b32 s9, v255, 35
	s_waitcnt lgkmcnt(0)
	s_add_u32 s7, s4, s8
	s_addc_u32 s8, s5, s9
	s_and_b32 s0, s69, 1
	s_lshl_b32 s4, s0, 2
	s_ashr_i32 s5, s33, 7
	s_lshl_b32 s9, s79, 5
	s_add_i32 s4, s5, s4
	s_lshl_b32 s5, s2, 6
	s_and_b32 s9, s9, 32
	s_or_b32 s5, s9, s5
	s_bfe_u32 s3, s69, 0x30001
	v_and_or_b32 v119, v154, 31, s5
	v_lshl_or_b32 v118, s3, 11, v119
	v_readlane_b32 s10, v254, 60
	v_lshlrev_b32_e32 v0, 10, v118
	v_readlane_b32 s11, v254, 61
	s_lshl_b32 s42, s4, 6
	v_lshrrev_b32_e32 v2, 5, v153
	v_lshl_add_u64 v[4:5], s[10:11], 0, v[0:1]
	s_ashr_i32 s43, s42, 31
	v_lshl_add_u64 v[4:5], s[42:43], 1, v[4:5]
	v_lshlrev_b32_e32 v0, 4, v2
	s_ashr_i32 s5, s4, 31
	v_lshl_add_u64 v[4:5], v[4:5], 0, v[0:1]
	s_lshl_b64 s[4:5], s[4:5], 2
	global_load_dwordx4 v[66:69], v[4:5], off
	global_load_dwordx4 v[70:73], v[4:5], off offset:32
	global_load_dwordx4 v[74:77], v[4:5], off offset:64
	global_load_dwordx4 v[78:81], v[4:5], off offset:96
	s_add_u32 s4, s7, s4
	s_addc_u32 s5, s8, s5
	global_load_dword v0, v1, s[4:5]
	v_sub_u32_e64 v3, 29, s6 clamp
	s_min_u32 s4, s6, 29
	v_readfirstlane_b32 s5, v3
	s_max_u32 s5, s2, s5
	s_add_i32 s4, s4, s5
	s_sub_i32 s10, s4, 28
	s_cmp_lt_u32 s10, 2
	v_readfirstlane_b32 s4, v3
	s_cbranch_scc1 .LBB0_3616
	s_and_b32 s11, s10, -2
	s_add_i32 s5, s4, 1
	s_mov_b32 s6, 0
	s_mov_b32 s12, s11
	s_mov_b64 s[8:9], s[4:5]
	s_mov_b32 s7, s6

.LBB0_3622:
	s_cmp_eq_u32 s99, 0
	s_cbranch_scc1 .Lstag_0
	s_sleep 8
